# non-temporal policy on the output row stores (plus early scanner loads before the barrier, DPP-based prep kernel, faster gatherer polling)
# speedup vs baseline: 1.0461x; 1.0392x over previous
_Z11prep_kernelPKfS0_PfPDv4_DF16_:
	s_load_dwordx4 s[4:7], s[0:1], 0x0
	s_load_dwordx4 s[8:11], s[0:1], 0x10
	s_lshl_b32 s2, s2, 8
	v_add_u32_e32 v2, s2, v0
	v_lshrrev_b32_e32 v12, 5, v2
	s_movk_i32 s3, 0x2710
	v_cmp_gt_u32_e32 vcc, s3, v12
	s_and_saveexec_b64 s[12:13], vcc
	s_cbranch_execz .Lprep_end
	v_and_b32_e32 v14, 31, v2
	v_lshlrev_b32_e32 v1, 4, v14
	v_lshlrev_b32_e32 v3, 4, v2
	s_waitcnt lgkmcnt(0)
	global_load_dwordx4 v[4:7], v1, s[6:7]
	global_load_dwordx4 v[8:11], v3, s[4:5]
	v_lshlrev_b32_e32 v13, 3, v2
	v_lshlrev_b32_e32 v15, 2, v12
	s_waitcnt vmcnt(0)
	v_mul_f32_e32 v5, v9, v5
	v_fmac_f32_e32 v5, v8, v4
	v_fmac_f32_e32 v5, v10, v6
	v_fmac_f32_e32 v5, v11, v7
	v_cvt_pk_f16_f32 v6, v8, v9
	v_cvt_pk_f16_f32 v7, v10, v11
	global_store_dwordx2 v13, v[6:7], s[10:11]
	v_add_f32_dpp v5, v5, v5 quad_perm:[1,0,3,2] row_mask:0xf bank_mask:0xf
	s_nop 1
	v_add_f32_dpp v5, v5, v5 quad_perm:[2,3,0,1] row_mask:0xf bank_mask:0xf
	s_nop 1
	v_add_f32_dpp v5, v5, v5 row_half_mirror row_mask:0xf bank_mask:0xf
	s_nop 1
	v_add_f32_dpp v5, v5, v5 row_mirror row_mask:0xf bank_mask:0xf
	s_nop 1
	v_add_f32_dpp v5, v5, v5 row_bcast:15 row_mask:0xa bank_mask:0xf
	v_cmp_eq_u32_e32 vcc, 16, v14
	s_and_b64 exec, exec, vcc
	global_store_dword v15, v5, s[8:9]

	.amdhsa_kernel _Z11prep_kernelPKfS0_PfPDv4_DF16_
		.amdhsa_group_segment_fixed_size 0
		.amdhsa_private_segment_fixed_size 0
		.amdhsa_kernarg_size 288
		.amdhsa_user_sgpr_count 2
		.amdhsa_user_sgpr_dispatch_ptr 0
		.amdhsa_user_sgpr_queue_ptr 0
		.amdhsa_user_sgpr_kernarg_segment_ptr 1
		.amdhsa_user_sgpr_dispatch_id 0
		.amdhsa_user_sgpr_kernarg_preload_length 0
		.amdhsa_user_sgpr_kernarg_preload_offset 0
		.amdhsa_user_sgpr_private_segment_size 0
		.amdhsa_uses_dynamic_stack 0
		.amdhsa_enable_private_segment 0
		.amdhsa_system_sgpr_workgroup_id_x 1
		.amdhsa_system_sgpr_workgroup_id_y 0
		.amdhsa_system_sgpr_workgroup_id_z 0
		.amdhsa_system_sgpr_workgroup_info 0
		.amdhsa_system_vgpr_workitem_id 0
		.amdhsa_next_free_vgpr 17
		.amdhsa_next_free_sgpr 14
		.amdhsa_accum_offset 20
		.amdhsa_reserve_vcc 1
		.amdhsa_float_round_mode_32 0
		.amdhsa_float_round_mode_16_64 0
		.amdhsa_float_denorm_mode_32 3
		.amdhsa_float_denorm_mode_16_64 3
		.amdhsa_dx10_clamp 1
		.amdhsa_ieee_mode 1
		.amdhsa_fp16_overflow 0
		.amdhsa_tg_split 0
		.amdhsa_exception_fp_ieee_invalid_op 0
		.amdhsa_exception_fp_denorm_src 0
		.amdhsa_exception_fp_ieee_div_zero 0
		.amdhsa_exception_fp_ieee_overflow 0
		.amdhsa_exception_fp_ieee_underflow 0
		.amdhsa_exception_fp_ieee_inexact 0
		.amdhsa_exception_int_div_zero 0
	.end_amdhsa_kernel

.Lfunc_end0:
	.size	_Z11prep_kernelPKfS0_PfPDv4_DF16_, .Lfunc_end0-_Z11prep_kernelPKfS0_PfPDv4_DF16_
	.set _Z11prep_kernelPKfS0_PfPDv4_DF16_.num_vgpr, 17
	.set _Z11prep_kernelPKfS0_PfPDv4_DF16_.num_agpr, 0
	.set _Z11prep_kernelPKfS0_PfPDv4_DF16_.numbered_sgpr, 14
	.set _Z11prep_kernelPKfS0_PfPDv4_DF16_.num_named_barrier, 0
	.set _Z11prep_kernelPKfS0_PfPDv4_DF16_.private_seg_size, 0
	.set _Z11prep_kernelPKfS0_PfPDv4_DF16_.uses_vcc, 1
	.set _Z11prep_kernelPKfS0_PfPDv4_DF16_.uses_flat_scratch, 0
	.set _Z11prep_kernelPKfS0_PfPDv4_DF16_.has_dyn_sized_stack, 0
	.set _Z11prep_kernelPKfS0_PfPDv4_DF16_.has_recursion, 0
	.set _Z11prep_kernelPKfS0_PfPDv4_DF16_.has_indirect_call, 0

_Z11attn_kernelPKfS0_PKDv8_DF16_S0_Pfi:
	s_load_dwordx2 s[28:29], s[0:1], 0x0
	v_cmp_gt_u32_e32 vcc, 8, v0
	s_and_saveexec_b64 s[4:5], vcc
	v_lshlrev_b32_e32 v1, 2, v0
	v_mov_b32_e32 v2, 0
	ds_write_b32 v1, v2 offset:36864
	s_or_b64 exec, exec, s[4:5]
	s_load_dword s33, s[0:1], 0x28
	v_bfe_u32 v1, v0, 6, 2
	v_lshl_or_b32 v82, s2, 2, v1
	v_readfirstlane_b32 s34, v0
	s_cmp_gt_u32 s34, 0xff
	s_cbranch_scc1 .Lsc_early_skip
	v_and_b32_e32 v3, 63, v0
	v_lshlrev_b32_e32 v2, 4, v3
	s_lshr_b32 s35, s34, 6
	s_lshl_b32 s37, s2, 2
	s_add_u32 s37, s37, s35
	s_and_b32 s47, s37, 1
	s_lshl_b32 s47, s47, 2
	s_mul_i32 s38, s37, 0x9c40
	s_lshl_b32 s40, s47, 4
	s_sub_u32 s38, s38, s40
	v_max_u32_e32 v12, s47, v3
	v_lshlrev_b32_e32 v12, 4, v12
	s_waitcnt lgkmcnt(0)
	s_and_b32 s29, s29, 0xffff
	s_mov_b32 s30, 0x17d78400
	s_mov_b32 s31, 0x20000
	buffer_load_dwordx4 v[100:103], v12, s[28:31], s38 offen nt
	s_add_u32 s40, s38, 0x400
	buffer_load_dwordx4 v[104:107], v2, s[28:31], s40 offen nt
	s_add_u32 s40, s38, 0x800
	buffer_load_dwordx4 v[108:111], v2, s[28:31], s40 offen nt
	s_add_u32 s40, s38, 0xc00
	buffer_load_dwordx4 v[112:115], v2, s[28:31], s40 offen nt
	s_add_u32 s40, s38, 0x1000
	buffer_load_dwordx4 v[116:119], v2, s[28:31], s40 offen nt
	s_add_u32 s40, s38, 0x1400
	buffer_load_dwordx4 v[120:123], v2, s[28:31], s40 offen nt
	s_add_u32 s40, s38, 0x1800
	buffer_load_dwordx4 v[124:127], v2, s[28:31], s40 offen nt
	s_add_u32 s40, s38, 0x1c00
	buffer_load_dwordx4 v[128:131], v2, s[28:31], s40 offen nt
	s_add_u32 s40, s38, 0x2000
	buffer_load_dwordx4 v[132:135], v2, s[28:31], s40 offen nt
	s_add_u32 s40, s38, 0x2400
	buffer_load_dwordx4 v[136:139], v2, s[28:31], s40 offen nt
	s_add_u32 s40, s38, 0x2800
	buffer_load_dwordx4 v[140:143], v2, s[28:31], s40 offen nt
	s_add_u32 s40, s38, 0x2c00
	buffer_load_dwordx4 v[144:147], v2, s[28:31], s40 offen nt
	s_add_u32 s40, s38, 0x3000
	buffer_load_dwordx4 v[148:151], v2, s[28:31], s40 offen nt
	s_add_u32 s40, s38, 0x3400
	buffer_load_dwordx4 v[152:155], v2, s[28:31], s40 offen nt
	s_add_u32 s40, s38, 0x3800
	buffer_load_dwordx4 v[156:159], v2, s[28:31], s40 offen nt
	s_add_u32 s40, s38, 0x3c00
	buffer_load_dwordx4 v[160:163], v2, s[28:31], s40 offen nt
	s_add_u32 s40, s38, 0x4000
	buffer_load_dwordx4 v[164:167], v2, s[28:31], s40 offen nt
	s_add_u32 s40, s38, 0x4400
	buffer_load_dwordx4 v[168:171], v2, s[28:31], s40 offen nt
	s_add_u32 s40, s38, 0x4800
	buffer_load_dwordx4 v[172:175], v2, s[28:31], s40 offen nt
	s_add_u32 s40, s38, 0x4c00
	buffer_load_dwordx4 v[176:179], v2, s[28:31], s40 offen nt
.Lsc_early_skip:
	s_waitcnt lgkmcnt(0)
	s_barrier
	v_cmp_gt_i32_e32 vcc, s33, v82
	s_and_saveexec_b64 s[4:5], vcc
	s_cbranch_execz .LBB1_384
	s_abs_i32 s3, s33
	v_cvt_f32_u32_e32 v2, s3
	s_movk_i32 s4, 0xff
	v_sub_u32_e32 v3, 0x270f, v82
	v_cmp_lt_u32_e32 vcc, s4, v0
	v_rcp_iflag_f32_e32 v2, v2
	v_sub_u32_e32 v5, 0, v3
	s_sub_i32 s4, 0, s3
	v_xor_b32_e32 v4, s33, v3
	v_mul_f32_e32 v2, 0x4f7ffffe, v2
	v_cvt_u32_f32_e32 v2, v2
	v_max_i32_e32 v3, v3, v5
	v_ashrrev_i32_e32 v4, 31, v4
	v_mul_lo_u32 v5, s4, v2
	v_mul_hi_u32 v5, v2, v5
	v_add_u32_e32 v2, v2, v5
	v_mul_hi_u32 v2, v3, v2
	v_mul_lo_u32 v5, v2, s3
	v_sub_u32_e32 v3, v3, v5
	v_add_u32_e32 v5, 1, v2
	v_cmp_le_u32_e64 s[4:5], s3, v3
	v_and_b32_e32 v83, 63, v0
	s_nop 0
	v_cndmask_b32_e64 v2, v2, v5, s[4:5]
	v_subrev_u32_e32 v5, s3, v3
	v_cndmask_b32_e64 v3, v3, v5, s[4:5]
	v_add_u32_e32 v5, 1, v2
	v_cmp_le_u32_e64 s[4:5], s3, v3
	s_nop 1
	v_cndmask_b32_e64 v2, v2, v5, s[4:5]
	v_xor_b32_e32 v2, v2, v4
	v_sub_u32_e32 v84, v2, v4
	s_and_saveexec_b64 s[4:5], vcc
	s_xor_b64 s[30:31], exec, s[4:5]
	s_cbranch_execz .LBB1_217
	v_cmp_lt_i32_e32 vcc, -1, v84
	s_and_saveexec_b64 s[34:35], vcc
	s_cbranch_execz .LBB1_216
	s_load_dwordx8 s[20:27], s[0:1], 0x8
	v_and_b32_e32 v69, 15, v0
	v_mov_b32_e32 v0, 0x8000
	v_lshrrev_b32_e32 v67, 4, v83
	v_lshl_or_b32 v88, v1, 10, v0
	s_mul_i32 s3, s2, 0x2710
	v_mul_u32_u24_e32 v0, 0x9c4, v1
	v_lshl_or_b32 v89, v69, 2, v67
	v_add3_u32 v90, s3, v0, v83
	v_lshlrev_b32_e32 v0, 2, v1
	v_mov_b32_e32 v2, 0x9000
	v_lshl_or_b32 v91, s2, 4, v0
	v_lshlrev_b32_e32 v0, 3, v89
	v_mov_b32_e32 v32, 0
	v_lshl_or_b32 v65, v1, 3, v2
	v_or_b32_e32 v2, 0x1e00, v0
	v_mov_b32_e32 v3, v32
	s_waitcnt lgkmcnt(0)
	v_lshl_add_u64 v[34:35], s[20:21], 0, v[2:3]
	v_or_b32_e32 v2, 0x1c00, v0
	v_lshl_add_u64 v[36:37], s[20:21], 0, v[2:3]
	v_or_b32_e32 v2, 0x1a00, v0
	v_lshl_add_u64 v[38:39], s[20:21], 0, v[2:3]
	v_or_b32_e32 v2, 0x1800, v0
	v_lshl_add_u64 v[40:41], s[20:21], 0, v[2:3]
	v_or_b32_e32 v2, 0x1600, v0
	v_lshl_add_u64 v[42:43], s[20:21], 0, v[2:3]
	v_or_b32_e32 v2, 0x1400, v0
	v_lshlrev_b32_e32 v63, 12, v1
	v_lshl_add_u64 v[44:45], s[20:21], 0, v[2:3]
	v_or_b32_e32 v2, 0x1200, v0
	v_mov_b32_e32 v1, v32
	v_lshl_or_b32 v71, v83, 3, v63
	v_lshl_or_b32 v73, v67, 3, v63
	v_lshl_add_u64 v[46:47], s[20:21], 0, v[2:3]
	v_or_b32_e32 v2, 0x1000, v0
	v_lshl_add_u64 v[50:51], s[20:21], 0, v[0:1]
	v_mbcnt_lo_u32_b32 v0, -1, 0
	v_or_b32_e32 v75, 4, v67
	v_or_b32_e32 v77, 8, v67
	v_or_b32_e32 v78, 12, v67
	v_or_b32_e32 v79, 16, v67
	v_or_b32_e32 v80, 20, v67
	v_or_b32_e32 v81, 24, v67
	v_or_b32_e32 v85, 28, v67
	v_or_b32_e32 v86, 64, v83
	v_or_b32_e32 v87, 0x4000, v63
	v_cmp_lt_u32_e64 s[0:1], 15, v83
	s_mul_i32 s39, s33, 0x9c4
	s_lshl_b32 s48, s33, 2
	v_or_b32_e32 v92, 0x200, v71
	v_or_b32_e32 v93, 0x204, v71
	v_or_b32_e32 v94, 0x100, v73
	v_lshl_add_u64 v[48:49], s[20:21], 0, v[2:3]
	s_mov_b32 s51, 0
	s_mov_b64 s[36:37], 0
	s_movk_i32 s49, 0x81
	s_mov_b32 s50, 0xff800000
	s_mov_b32 s38, 0x38d1b717
	v_mov_b32_e32 v95, 0xff800000
	v_mbcnt_hi_u32_b32 v96, -1, v0
	v_mov_b32_e32 v136, 0
	v_mov_b32_e32 v137, 0
	v_mov_b32_e32 v138, 0
	v_mov_b32_e32 v139, 0
	v_mov_b32_e32 v140, 0
	v_mov_b32_e32 v141, 0
	v_mov_b32_e32 v142, 0
	v_mov_b32_e32 v143, 0
	v_mov_b32_e32 v144, 0
	v_mov_b32_e32 v145, 0
	v_mov_b32_e32 v146, 0
	v_mov_b32_e32 v147, 0
	v_mov_b32_e32 v148, 0
	v_mov_b32_e32 v149, 0
	v_mov_b32_e32 v150, 0
	v_mov_b32_e32 v151, 0
	v_mov_b32_e32 v152, 0
	v_mov_b32_e32 v153, 0
	v_mov_b32_e32 v154, 0
	v_mov_b32_e32 v155, 0
	v_mov_b32_e32 v156, 0
	v_mov_b32_e32 v157, 0
	v_mov_b32_e32 v158, 0
	v_mov_b32_e32 v159, 0
	v_mov_b32_e32 v160, 0
	v_mov_b32_e32 v161, 0
	v_mov_b32_e32 v162, 0
	v_mov_b32_e32 v163, 0
	v_mov_b32_e32 v164, 0
	v_mov_b32_e32 v165, 0
	v_mov_b32_e32 v166, 0
	v_mov_b32_e32 v167, 0
	v_mov_b32_e32 v168, 0
	v_mov_b32_e32 v169, 0
	v_mov_b32_e32 v170, 0
	v_mov_b32_e32 v171, 0
	v_mov_b32_e32 v172, 0
	v_mov_b32_e32 v173, 0
	v_mov_b32_e32 v174, 0
	v_mov_b32_e32 v175, 0
	v_mov_b32_e32 v176, 0
	v_mov_b32_e32 v177, 0
	v_mov_b32_e32 v178, 0
	v_mov_b32_e32 v179, 0
	v_mov_b32_e32 v180, 0
	v_mov_b32_e32 v181, 0
	v_mov_b32_e32 v182, 0
	v_mov_b32_e32 v183, 0
	v_mov_b32_e32 v184, 0
	v_mov_b32_e32 v185, 0
	v_mov_b32_e32 v186, 0
	v_mov_b32_e32 v187, 0
	v_mov_b32_e32 v188, 0
	v_mov_b32_e32 v189, 0
	v_mov_b32_e32 v190, 0
	v_mov_b32_e32 v191, 0
	v_mov_b32_e32 v192, 0
	v_mov_b32_e32 v193, 0
	v_mov_b32_e32 v194, 0
	v_mov_b32_e32 v195, 0
	v_mov_b32_e32 v196, 0
	v_mov_b32_e32 v197, 0
	v_mov_b32_e32 v198, 0
	v_mov_b32_e32 v199, 0
	s_branch .LBB1_9

.LBB1_8:
	s_or_b64 exec, exec, s[2:3]
	v_lshl_or_b32 v2, v97, 6, v89
	v_ashrrev_i32_e32 v3, 31, v2
	s_add_i32 s2, s51, 1
	v_cmp_eq_u32_e32 vcc, s51, v84
	v_lshl_add_u64 v[2:3], v[2:3], 3, s[26:27]
	v_add_u32_e32 v90, s39, v90
	v_add_u32_e32 v91, s48, v91
	s_or_b64 s[36:37], vcc, s[36:37]
	s_mov_b32 s51, s2
	global_store_dwordx2 v[2:3], v[0:1], off nt
	s_andn2_b64 exec, exec, s[36:37]
	s_cbranch_execz .LBB1_216

.LBB1_11:
	s_sleep 1
	ds_read_b32 v0, v6
	s_waitcnt lgkmcnt(0)
	v_cmp_ne_u32_e32 vcc, 0, v0
	s_or_b64 s[4:5], vcc, s[4:5]
	s_andn2_b64 exec, exec, s[4:5]
	s_cbranch_execnz .LBB1_11
	s_or_b64 exec, exec, s[4:5]

.LBB1_217:
	s_andn2_saveexec_b64 s[0:1], s[30:31]
	s_cbranch_execz .LBB1_384
	v_readfirstlane_b32 s34, v1
	v_readfirstlane_b32 s37, v82
	v_readfirstlane_b32 s36, v84
	v_and_b32_e32 v3, 63, v0
	v_lshlrev_b32_e32 v2, 4, v3
	s_cmp_lt_i32 s36, 0
	s_cbranch_scc1 .LBB1_384
	s_waitcnt lgkmcnt(0)
	s_and_b32 s29, s29, 0xffff
	s_mov_b32 s30, 0x17d78400
	s_mov_b32 s31, 0x20000
	s_mov_b32 s35, 0
	s_movk_i32 s7, 0x80
	s_mov_b32 s9, 0x7fffffff
	s_lshl_b32 s44, s34, 12
	s_add_u32 s44, s44, 0x4000
	s_lshl_b32 s45, s34, 10
	s_add_u32 s45, s45, 0x8000
	s_lshl_b32 s46, s34, 3
	s_add_u32 s46, s46, 0x9000
	s_and_b32 s47, s37, 1
	s_lshl_b32 s47, s47, 2
	s_mul_i32 s38, s37, 0x9c40
	s_lshl_b32 s40, s47, 4
	s_sub_u32 s38, s38, s40
	v_max_u32_e32 v12, s47, v3
	v_lshlrev_b32_e32 v12, 4, v12
.Lsc_row:
	v_subrev_u32_e32 v8, s47, v3
	v_lshlrev_b32_e32 v8, 2, v8
	s_add_i32 s41, s47, 3
	v_min_u32_e32 v4, s41, v3
	v_lshlrev_b32_e32 v4, 4, v4
	s_lshl_b64 s[48:49], -1, s47
	s_add_i32 s41, s47, 4
	s_lshl_b64 s[50:51], 1, s41
	s_sub_u32 s50, s50, 1
	s_and_b32 s41, s35, 1
	s_lshl_b32 s40, s41, 11
	s_add_u32 s40, s40, s44
	v_mov_b32_e32 v9, s40
	s_lshl_b32 s40, s41, 9
	s_add_u32 s40, s40, s45
	v_mov_b32_e32 v10, s40
	s_lshl_b32 s40, s41, 2
	s_add_u32 s40, s40, s46
	v_mov_b32_e32 v11, s40
	s_cmp_lt_i32 s35, s36
	s_cbranch_scc0 .Lsc_nonext
	s_add_i32 s52, s37, s33
	s_and_b32 s53, s52, 1
	s_lshl_b32 s53, s53, 2
	s_mul_i32 s39, s52, 0x9c40
	s_lshl_b32 s40, s53, 4
	s_sub_u32 s39, s39, s40
	v_max_u32_e32 v5, s53, v3
	v_lshlrev_b32_e32 v5, 4, v5
	v_mov_b32_e32 v6, v2
	s_add_i32 s40, s53, 3
	v_min_u32_e32 v7, s40, v3
	v_lshlrev_b32_e32 v7, 4, v7
	s_branch .Lsc_gotnext

.Lsc_go:
	s_mov_b32 s42, 0
	s_waitcnt vmcnt(19)
	v_or3_b32 v12, v100, v101, v102
	v_bitop3_b32 v12, v12, s9, v103 bitop3:0xc8
	v_cmp_ne_u32_e32 vcc, 0, v12
	s_and_b64 vcc, vcc, s[48:49]
	s_cbranch_vccz .Lsc_s0
	s_nop 0
	v_mbcnt_lo_u32_b32 v13, vcc_lo, 0
	v_mbcnt_hi_u32_b32 v13, vcc_hi, v13
	v_add_u32_e32 v13, s42, v13
	v_cmp_gt_i32_e64 s[0:1], s7, v13
	s_and_b64 s[4:5], vcc, s[0:1]
	s_and_saveexec_b64 s[0:1], s[4:5]
	v_lshl_add_u32 v14, v13, 4, v9
	v_lshl_add_u32 v15, v13, 2, v10
	v_mov_b32_e32 v13, v8
	ds_write_b128 v14, v[100:103]
	ds_write_b32 v15, v13
	s_mov_b64 exec, -1
	s_bcnt1_i32_b64 s40, vcc
	s_add_i32 s42, s42, s40
.Lsc_s0:
	s_add_u32 s40, s38, 0x5000
	buffer_load_dwordx4 v[100:103], v2, s[28:31], s40 offen nt
	s_waitcnt vmcnt(19)
	v_or3_b32 v12, v104, v105, v106
	v_bitop3_b32 v12, v12, s9, v107 bitop3:0xc8
	v_cmp_ne_u32_e32 vcc, 0, v12
	s_cbranch_vccz .Lsc_s1
	s_nop 0
	v_mbcnt_lo_u32_b32 v13, vcc_lo, 0
	v_mbcnt_hi_u32_b32 v13, vcc_hi, v13
	v_add_u32_e32 v13, s42, v13
	v_cmp_gt_i32_e64 s[0:1], s7, v13
	s_and_b64 s[4:5], vcc, s[0:1]
	s_and_saveexec_b64 s[0:1], s[4:5]
	v_lshl_add_u32 v14, v13, 4, v9
	v_lshl_add_u32 v15, v13, 2, v10
	v_add_u32_e32 v13, 0x100, v8
	ds_write_b128 v14, v[104:107]
	ds_write_b32 v15, v13
	s_mov_b64 exec, -1
	s_bcnt1_i32_b64 s40, vcc
	s_add_i32 s42, s42, s40
.Lsc_s1:
	s_add_u32 s40, s38, 0x5400
	buffer_load_dwordx4 v[104:107], v2, s[28:31], s40 offen nt
	s_waitcnt vmcnt(19)
	v_or3_b32 v12, v108, v109, v110
	v_bitop3_b32 v12, v12, s9, v111 bitop3:0xc8
	v_cmp_ne_u32_e32 vcc, 0, v12
	s_cbranch_vccz .Lsc_s2
	s_nop 0
	v_mbcnt_lo_u32_b32 v13, vcc_lo, 0
	v_mbcnt_hi_u32_b32 v13, vcc_hi, v13
	v_add_u32_e32 v13, s42, v13
	v_cmp_gt_i32_e64 s[0:1], s7, v13
	s_and_b64 s[4:5], vcc, s[0:1]
	s_and_saveexec_b64 s[0:1], s[4:5]
	v_lshl_add_u32 v14, v13, 4, v9
	v_lshl_add_u32 v15, v13, 2, v10
	v_add_u32_e32 v13, 0x200, v8
	ds_write_b128 v14, v[108:111]
	ds_write_b32 v15, v13
	s_mov_b64 exec, -1
	s_bcnt1_i32_b64 s40, vcc
	s_add_i32 s42, s42, s40
.Lsc_s2:
	s_add_u32 s40, s38, 0x5800
	buffer_load_dwordx4 v[108:111], v2, s[28:31], s40 offen nt
	s_waitcnt vmcnt(19)
	v_or3_b32 v12, v112, v113, v114
	v_bitop3_b32 v12, v12, s9, v115 bitop3:0xc8
	v_cmp_ne_u32_e32 vcc, 0, v12
	s_cbranch_vccz .Lsc_s3
	s_nop 0
	v_mbcnt_lo_u32_b32 v13, vcc_lo, 0
	v_mbcnt_hi_u32_b32 v13, vcc_hi, v13
	v_add_u32_e32 v13, s42, v13
	v_cmp_gt_i32_e64 s[0:1], s7, v13
	s_and_b64 s[4:5], vcc, s[0:1]
	s_and_saveexec_b64 s[0:1], s[4:5]
	v_lshl_add_u32 v14, v13, 4, v9
	v_lshl_add_u32 v15, v13, 2, v10
	v_add_u32_e32 v13, 0x300, v8
	ds_write_b128 v14, v[112:115]
	ds_write_b32 v15, v13
	s_mov_b64 exec, -1
	s_bcnt1_i32_b64 s40, vcc
	s_add_i32 s42, s42, s40
.Lsc_s3:
	s_add_u32 s40, s38, 0x5c00
	buffer_load_dwordx4 v[112:115], v2, s[28:31], s40 offen nt
	s_waitcnt vmcnt(19)
	v_or3_b32 v12, v116, v117, v118
	v_bitop3_b32 v12, v12, s9, v119 bitop3:0xc8
	v_cmp_ne_u32_e32 vcc, 0, v12
	s_cbranch_vccz .Lsc_s4
	s_nop 0
	v_mbcnt_lo_u32_b32 v13, vcc_lo, 0
	v_mbcnt_hi_u32_b32 v13, vcc_hi, v13
	v_add_u32_e32 v13, s42, v13
	v_cmp_gt_i32_e64 s[0:1], s7, v13
	s_and_b64 s[4:5], vcc, s[0:1]
	s_and_saveexec_b64 s[0:1], s[4:5]
	v_lshl_add_u32 v14, v13, 4, v9
	v_lshl_add_u32 v15, v13, 2, v10
	v_add_u32_e32 v13, 0x400, v8
	ds_write_b128 v14, v[116:119]
	ds_write_b32 v15, v13
	s_mov_b64 exec, -1
	s_bcnt1_i32_b64 s40, vcc
	s_add_i32 s42, s42, s40
.Lsc_s4:
	s_add_u32 s40, s38, 0x6000
	buffer_load_dwordx4 v[116:119], v2, s[28:31], s40 offen nt
	s_waitcnt vmcnt(19)
	v_or3_b32 v12, v120, v121, v122
	v_bitop3_b32 v12, v12, s9, v123 bitop3:0xc8
	v_cmp_ne_u32_e32 vcc, 0, v12
	s_cbranch_vccz .Lsc_s5
	s_nop 0
	v_mbcnt_lo_u32_b32 v13, vcc_lo, 0
	v_mbcnt_hi_u32_b32 v13, vcc_hi, v13
	v_add_u32_e32 v13, s42, v13
	v_cmp_gt_i32_e64 s[0:1], s7, v13
	s_and_b64 s[4:5], vcc, s[0:1]
	s_and_saveexec_b64 s[0:1], s[4:5]
	v_lshl_add_u32 v14, v13, 4, v9
	v_lshl_add_u32 v15, v13, 2, v10
	v_add_u32_e32 v13, 0x500, v8
	ds_write_b128 v14, v[120:123]
	ds_write_b32 v15, v13
	s_mov_b64 exec, -1
	s_bcnt1_i32_b64 s40, vcc
	s_add_i32 s42, s42, s40
.Lsc_s5:
	s_add_u32 s40, s38, 0x6400
	buffer_load_dwordx4 v[120:123], v2, s[28:31], s40 offen nt
	s_waitcnt vmcnt(19)
	v_or3_b32 v12, v124, v125, v126
	v_bitop3_b32 v12, v12, s9, v127 bitop3:0xc8
	v_cmp_ne_u32_e32 vcc, 0, v12
	s_cbranch_vccz .Lsc_s6
	s_nop 0
	v_mbcnt_lo_u32_b32 v13, vcc_lo, 0
	v_mbcnt_hi_u32_b32 v13, vcc_hi, v13
	v_add_u32_e32 v13, s42, v13
	v_cmp_gt_i32_e64 s[0:1], s7, v13
	s_and_b64 s[4:5], vcc, s[0:1]
	s_and_saveexec_b64 s[0:1], s[4:5]
	v_lshl_add_u32 v14, v13, 4, v9
	v_lshl_add_u32 v15, v13, 2, v10
	v_add_u32_e32 v13, 0x600, v8
	ds_write_b128 v14, v[124:127]
	ds_write_b32 v15, v13
	s_mov_b64 exec, -1
	s_bcnt1_i32_b64 s40, vcc
	s_add_i32 s42, s42, s40
.Lsc_s6:
	s_add_u32 s40, s38, 0x6800
	buffer_load_dwordx4 v[124:127], v2, s[28:31], s40 offen nt
	s_waitcnt vmcnt(19)
	v_or3_b32 v12, v128, v129, v130
	v_bitop3_b32 v12, v12, s9, v131 bitop3:0xc8
	v_cmp_ne_u32_e32 vcc, 0, v12
	s_cbranch_vccz .Lsc_s7
	s_nop 0
	v_mbcnt_lo_u32_b32 v13, vcc_lo, 0
	v_mbcnt_hi_u32_b32 v13, vcc_hi, v13
	v_add_u32_e32 v13, s42, v13
	v_cmp_gt_i32_e64 s[0:1], s7, v13
	s_and_b64 s[4:5], vcc, s[0:1]
	s_and_saveexec_b64 s[0:1], s[4:5]
	v_lshl_add_u32 v14, v13, 4, v9
	v_lshl_add_u32 v15, v13, 2, v10
	v_add_u32_e32 v13, 0x700, v8
	ds_write_b128 v14, v[128:131]
	ds_write_b32 v15, v13
	s_mov_b64 exec, -1
	s_bcnt1_i32_b64 s40, vcc
	s_add_i32 s42, s42, s40
.Lsc_s7:
	s_add_u32 s40, s38, 0x6c00
	buffer_load_dwordx4 v[128:131], v2, s[28:31], s40 offen nt
	s_waitcnt vmcnt(19)
	v_or3_b32 v12, v132, v133, v134
	v_bitop3_b32 v12, v12, s9, v135 bitop3:0xc8
	v_cmp_ne_u32_e32 vcc, 0, v12
	s_cbranch_vccz .Lsc_s8
	s_nop 0
	v_mbcnt_lo_u32_b32 v13, vcc_lo, 0
	v_mbcnt_hi_u32_b32 v13, vcc_hi, v13
	v_add_u32_e32 v13, s42, v13
	v_cmp_gt_i32_e64 s[0:1], s7, v13
	s_and_b64 s[4:5], vcc, s[0:1]
	s_and_saveexec_b64 s[0:1], s[4:5]
	v_lshl_add_u32 v14, v13, 4, v9
	v_lshl_add_u32 v15, v13, 2, v10
	v_add_u32_e32 v13, 0x800, v8
	ds_write_b128 v14, v[132:135]
	ds_write_b32 v15, v13
	s_mov_b64 exec, -1
	s_bcnt1_i32_b64 s40, vcc
	s_add_i32 s42, s42, s40
.Lsc_s8:
	s_add_u32 s40, s38, 0x7000
	buffer_load_dwordx4 v[132:135], v2, s[28:31], s40 offen nt
	s_waitcnt vmcnt(19)
	v_or3_b32 v12, v136, v137, v138
	v_bitop3_b32 v12, v12, s9, v139 bitop3:0xc8
	v_cmp_ne_u32_e32 vcc, 0, v12
	s_cbranch_vccz .Lsc_s9
	s_nop 0
	v_mbcnt_lo_u32_b32 v13, vcc_lo, 0
	v_mbcnt_hi_u32_b32 v13, vcc_hi, v13
	v_add_u32_e32 v13, s42, v13
	v_cmp_gt_i32_e64 s[0:1], s7, v13
	s_and_b64 s[4:5], vcc, s[0:1]
	s_and_saveexec_b64 s[0:1], s[4:5]
	v_lshl_add_u32 v14, v13, 4, v9
	v_lshl_add_u32 v15, v13, 2, v10
	v_add_u32_e32 v13, 0x900, v8
	ds_write_b128 v14, v[136:139]
	ds_write_b32 v15, v13
	s_mov_b64 exec, -1
	s_bcnt1_i32_b64 s40, vcc
	s_add_i32 s42, s42, s40
.Lsc_s9:
	s_add_u32 s40, s38, 0x7400
	buffer_load_dwordx4 v[136:139], v2, s[28:31], s40 offen nt
	s_waitcnt vmcnt(19)
	v_or3_b32 v12, v140, v141, v142
	v_bitop3_b32 v12, v12, s9, v143 bitop3:0xc8
	v_cmp_ne_u32_e32 vcc, 0, v12
	s_cbranch_vccz .Lsc_s10
	s_nop 0
	v_mbcnt_lo_u32_b32 v13, vcc_lo, 0
	v_mbcnt_hi_u32_b32 v13, vcc_hi, v13
	v_add_u32_e32 v13, s42, v13
	v_cmp_gt_i32_e64 s[0:1], s7, v13
	s_and_b64 s[4:5], vcc, s[0:1]
	s_and_saveexec_b64 s[0:1], s[4:5]
	v_lshl_add_u32 v14, v13, 4, v9
	v_lshl_add_u32 v15, v13, 2, v10
	v_add_u32_e32 v13, 0xa00, v8
	ds_write_b128 v14, v[140:143]
	ds_write_b32 v15, v13
	s_mov_b64 exec, -1
	s_bcnt1_i32_b64 s40, vcc
	s_add_i32 s42, s42, s40
.Lsc_s10:
	s_add_u32 s40, s38, 0x7800
	buffer_load_dwordx4 v[140:143], v2, s[28:31], s40 offen nt
	s_waitcnt vmcnt(19)
	v_or3_b32 v12, v144, v145, v146
	v_bitop3_b32 v12, v12, s9, v147 bitop3:0xc8
	v_cmp_ne_u32_e32 vcc, 0, v12
	s_cbranch_vccz .Lsc_s11
	s_nop 0
	v_mbcnt_lo_u32_b32 v13, vcc_lo, 0
	v_mbcnt_hi_u32_b32 v13, vcc_hi, v13
	v_add_u32_e32 v13, s42, v13
	v_cmp_gt_i32_e64 s[0:1], s7, v13
	s_and_b64 s[4:5], vcc, s[0:1]
	s_and_saveexec_b64 s[0:1], s[4:5]
	v_lshl_add_u32 v14, v13, 4, v9
	v_lshl_add_u32 v15, v13, 2, v10
	v_add_u32_e32 v13, 0xb00, v8
	ds_write_b128 v14, v[144:147]
	ds_write_b32 v15, v13
	s_mov_b64 exec, -1
	s_bcnt1_i32_b64 s40, vcc
	s_add_i32 s42, s42, s40
.Lsc_s11:
	s_add_u32 s40, s38, 0x7c00
	buffer_load_dwordx4 v[144:147], v2, s[28:31], s40 offen nt
	s_waitcnt vmcnt(19)
	v_or3_b32 v12, v148, v149, v150
	v_bitop3_b32 v12, v12, s9, v151 bitop3:0xc8
	v_cmp_ne_u32_e32 vcc, 0, v12
	s_cbranch_vccz .Lsc_s12
	s_nop 0
	v_mbcnt_lo_u32_b32 v13, vcc_lo, 0
	v_mbcnt_hi_u32_b32 v13, vcc_hi, v13
	v_add_u32_e32 v13, s42, v13
	v_cmp_gt_i32_e64 s[0:1], s7, v13
	s_and_b64 s[4:5], vcc, s[0:1]
	s_and_saveexec_b64 s[0:1], s[4:5]
	v_lshl_add_u32 v14, v13, 4, v9
	v_lshl_add_u32 v15, v13, 2, v10
	v_add_u32_e32 v13, 0xc00, v8
	ds_write_b128 v14, v[148:151]
	ds_write_b32 v15, v13
	s_mov_b64 exec, -1
	s_bcnt1_i32_b64 s40, vcc
	s_add_i32 s42, s42, s40
.Lsc_s12:
	s_add_u32 s40, s38, 0x8000
	buffer_load_dwordx4 v[148:151], v2, s[28:31], s40 offen nt
	s_waitcnt vmcnt(19)
	v_or3_b32 v12, v152, v153, v154
	v_bitop3_b32 v12, v12, s9, v155 bitop3:0xc8
	v_cmp_ne_u32_e32 vcc, 0, v12
	s_cbranch_vccz .Lsc_s13
	s_nop 0
	v_mbcnt_lo_u32_b32 v13, vcc_lo, 0
	v_mbcnt_hi_u32_b32 v13, vcc_hi, v13
	v_add_u32_e32 v13, s42, v13
	v_cmp_gt_i32_e64 s[0:1], s7, v13
	s_and_b64 s[4:5], vcc, s[0:1]
	s_and_saveexec_b64 s[0:1], s[4:5]
	v_lshl_add_u32 v14, v13, 4, v9
	v_lshl_add_u32 v15, v13, 2, v10
	v_add_u32_e32 v13, 0xd00, v8
	ds_write_b128 v14, v[152:155]
	ds_write_b32 v15, v13
	s_mov_b64 exec, -1
	s_bcnt1_i32_b64 s40, vcc
	s_add_i32 s42, s42, s40
.Lsc_s13:
	s_add_u32 s40, s38, 0x8400
	buffer_load_dwordx4 v[152:155], v2, s[28:31], s40 offen nt
	s_waitcnt vmcnt(19)
	v_or3_b32 v12, v156, v157, v158
	v_bitop3_b32 v12, v12, s9, v159 bitop3:0xc8
	v_cmp_ne_u32_e32 vcc, 0, v12
	s_cbranch_vccz .Lsc_s14
	s_nop 0
	v_mbcnt_lo_u32_b32 v13, vcc_lo, 0
	v_mbcnt_hi_u32_b32 v13, vcc_hi, v13
	v_add_u32_e32 v13, s42, v13
	v_cmp_gt_i32_e64 s[0:1], s7, v13
	s_and_b64 s[4:5], vcc, s[0:1]
	s_and_saveexec_b64 s[0:1], s[4:5]
	v_lshl_add_u32 v14, v13, 4, v9
	v_lshl_add_u32 v15, v13, 2, v10
	v_add_u32_e32 v13, 0xe00, v8
	ds_write_b128 v14, v[156:159]
	ds_write_b32 v15, v13
	s_mov_b64 exec, -1
	s_bcnt1_i32_b64 s40, vcc
	s_add_i32 s42, s42, s40
.Lsc_s14:
	s_add_u32 s40, s38, 0x8800
	buffer_load_dwordx4 v[156:159], v2, s[28:31], s40 offen nt
	s_waitcnt vmcnt(19)
	v_or3_b32 v12, v160, v161, v162
	v_bitop3_b32 v12, v12, s9, v163 bitop3:0xc8
	v_cmp_ne_u32_e32 vcc, 0, v12
	s_cbranch_vccz .Lsc_s15
	s_nop 0
	v_mbcnt_lo_u32_b32 v13, vcc_lo, 0
	v_mbcnt_hi_u32_b32 v13, vcc_hi, v13
	v_add_u32_e32 v13, s42, v13
	v_cmp_gt_i32_e64 s[0:1], s7, v13
	s_and_b64 s[4:5], vcc, s[0:1]
	s_and_saveexec_b64 s[0:1], s[4:5]
	v_lshl_add_u32 v14, v13, 4, v9
	v_lshl_add_u32 v15, v13, 2, v10
	v_add_u32_e32 v13, 0xf00, v8
	ds_write_b128 v14, v[160:163]
	ds_write_b32 v15, v13
	s_mov_b64 exec, -1
	s_bcnt1_i32_b64 s40, vcc
	s_add_i32 s42, s42, s40
.Lsc_s15:
	s_add_u32 s40, s38, 0x8c00
	buffer_load_dwordx4 v[160:163], v2, s[28:31], s40 offen nt
	s_waitcnt vmcnt(19)
	v_or3_b32 v12, v164, v165, v166
	v_bitop3_b32 v12, v12, s9, v167 bitop3:0xc8
	v_cmp_ne_u32_e32 vcc, 0, v12
	s_cbranch_vccz .Lsc_s16
	s_nop 0
	v_mbcnt_lo_u32_b32 v13, vcc_lo, 0
	v_mbcnt_hi_u32_b32 v13, vcc_hi, v13
	v_add_u32_e32 v13, s42, v13
	v_cmp_gt_i32_e64 s[0:1], s7, v13
	s_and_b64 s[4:5], vcc, s[0:1]
	s_and_saveexec_b64 s[0:1], s[4:5]
	v_lshl_add_u32 v14, v13, 4, v9
	v_lshl_add_u32 v15, v13, 2, v10
	v_add_u32_e32 v13, 0x1000, v8
	ds_write_b128 v14, v[164:167]
	ds_write_b32 v15, v13
	s_mov_b64 exec, -1
	s_bcnt1_i32_b64 s40, vcc
	s_add_i32 s42, s42, s40
.Lsc_s16:
	s_add_u32 s40, s38, 0x9000
	buffer_load_dwordx4 v[164:167], v2, s[28:31], s40 offen nt
	s_waitcnt vmcnt(19)
	v_or3_b32 v12, v168, v169, v170
	v_bitop3_b32 v12, v12, s9, v171 bitop3:0xc8
	v_cmp_ne_u32_e32 vcc, 0, v12
	s_cbranch_vccz .Lsc_s17
	s_nop 0
	v_mbcnt_lo_u32_b32 v13, vcc_lo, 0
	v_mbcnt_hi_u32_b32 v13, vcc_hi, v13
	v_add_u32_e32 v13, s42, v13
	v_cmp_gt_i32_e64 s[0:1], s7, v13
	s_and_b64 s[4:5], vcc, s[0:1]
	s_and_saveexec_b64 s[0:1], s[4:5]
	v_lshl_add_u32 v14, v13, 4, v9
	v_lshl_add_u32 v15, v13, 2, v10
	v_add_u32_e32 v13, 0x1100, v8
	ds_write_b128 v14, v[168:171]
	ds_write_b32 v15, v13
	s_mov_b64 exec, -1
	s_bcnt1_i32_b64 s40, vcc
	s_add_i32 s42, s42, s40
.Lsc_s17:
	s_add_u32 s40, s38, 0x9400
	buffer_load_dwordx4 v[168:171], v2, s[28:31], s40 offen nt
	s_waitcnt vmcnt(19)
	v_or3_b32 v12, v172, v173, v174
	v_bitop3_b32 v12, v12, s9, v175 bitop3:0xc8
	v_cmp_ne_u32_e32 vcc, 0, v12
	s_cbranch_vccz .Lsc_s18
	s_nop 0
	v_mbcnt_lo_u32_b32 v13, vcc_lo, 0
	v_mbcnt_hi_u32_b32 v13, vcc_hi, v13
	v_add_u32_e32 v13, s42, v13
	v_cmp_gt_i32_e64 s[0:1], s7, v13
	s_and_b64 s[4:5], vcc, s[0:1]
	s_and_saveexec_b64 s[0:1], s[4:5]
	v_lshl_add_u32 v14, v13, 4, v9
	v_lshl_add_u32 v15, v13, 2, v10
	v_add_u32_e32 v13, 0x1200, v8
	ds_write_b128 v14, v[172:175]
	ds_write_b32 v15, v13
	s_mov_b64 exec, -1
	s_bcnt1_i32_b64 s40, vcc
	s_add_i32 s42, s42, s40
.Lsc_s18:
	s_add_u32 s40, s38, 0x9800
	buffer_load_dwordx4 v[172:175], v2, s[28:31], s40 offen nt
	s_waitcnt vmcnt(19)
	v_or3_b32 v12, v176, v177, v178
	v_bitop3_b32 v12, v12, s9, v179 bitop3:0xc8
	v_cmp_ne_u32_e32 vcc, 0, v12
	s_cbranch_vccz .Lsc_s19
	s_nop 0
	v_mbcnt_lo_u32_b32 v13, vcc_lo, 0
	v_mbcnt_hi_u32_b32 v13, vcc_hi, v13
	v_add_u32_e32 v13, s42, v13
	v_cmp_gt_i32_e64 s[0:1], s7, v13
	s_and_b64 s[4:5], vcc, s[0:1]
	s_and_saveexec_b64 s[0:1], s[4:5]
	v_lshl_add_u32 v14, v13, 4, v9
	v_lshl_add_u32 v15, v13, 2, v10
	v_add_u32_e32 v13, 0x1300, v8
	ds_write_b128 v14, v[176:179]
	ds_write_b32 v15, v13
	s_mov_b64 exec, -1
	s_bcnt1_i32_b64 s40, vcc
	s_add_i32 s42, s42, s40
.Lsc_s19:
	s_add_u32 s40, s38, 0x9c00
	buffer_load_dwordx4 v[176:179], v4, s[28:31], s40 offen nt
	s_waitcnt vmcnt(19)
	v_or3_b32 v12, v100, v101, v102
	v_bitop3_b32 v12, v12, s9, v103 bitop3:0xc8
	v_cmp_ne_u32_e32 vcc, 0, v12
	s_cbranch_vccz .Lsc_s20
	s_nop 0
	v_mbcnt_lo_u32_b32 v13, vcc_lo, 0
	v_mbcnt_hi_u32_b32 v13, vcc_hi, v13
	v_add_u32_e32 v13, s42, v13
	v_cmp_gt_i32_e64 s[0:1], s7, v13
	s_and_b64 s[4:5], vcc, s[0:1]
	s_and_saveexec_b64 s[0:1], s[4:5]
	v_lshl_add_u32 v14, v13, 4, v9
	v_lshl_add_u32 v15, v13, 2, v10
	v_add_u32_e32 v13, 0x1400, v8
	ds_write_b128 v14, v[100:103]
	ds_write_b32 v15, v13
	s_mov_b64 exec, -1
	s_bcnt1_i32_b64 s40, vcc
	s_add_i32 s42, s42, s40
.Lsc_s20:
	s_mov_b32 s40, s39
	buffer_load_dwordx4 v[100:103], v5, s[28:31], s40 offen nt
	s_waitcnt vmcnt(19)
	v_or3_b32 v12, v104, v105, v106
	v_bitop3_b32 v12, v12, s9, v107 bitop3:0xc8
	v_cmp_ne_u32_e32 vcc, 0, v12
	s_cbranch_vccz .Lsc_s21
	s_nop 0
	v_mbcnt_lo_u32_b32 v13, vcc_lo, 0
	v_mbcnt_hi_u32_b32 v13, vcc_hi, v13
	v_add_u32_e32 v13, s42, v13
	v_cmp_gt_i32_e64 s[0:1], s7, v13
	s_and_b64 s[4:5], vcc, s[0:1]
	s_and_saveexec_b64 s[0:1], s[4:5]
	v_lshl_add_u32 v14, v13, 4, v9
	v_lshl_add_u32 v15, v13, 2, v10
	v_add_u32_e32 v13, 0x1500, v8
	ds_write_b128 v14, v[104:107]
	ds_write_b32 v15, v13
	s_mov_b64 exec, -1
	s_bcnt1_i32_b64 s40, vcc
	s_add_i32 s42, s42, s40
.Lsc_s21:
	s_add_u32 s40, s39, 0x400
	buffer_load_dwordx4 v[104:107], v6, s[28:31], s40 offen nt
	s_waitcnt vmcnt(19)
	v_or3_b32 v12, v108, v109, v110
	v_bitop3_b32 v12, v12, s9, v111 bitop3:0xc8
	v_cmp_ne_u32_e32 vcc, 0, v12
	s_cbranch_vccz .Lsc_s22
	s_nop 0
	v_mbcnt_lo_u32_b32 v13, vcc_lo, 0
	v_mbcnt_hi_u32_b32 v13, vcc_hi, v13
	v_add_u32_e32 v13, s42, v13
	v_cmp_gt_i32_e64 s[0:1], s7, v13
	s_and_b64 s[4:5], vcc, s[0:1]
	s_and_saveexec_b64 s[0:1], s[4:5]
	v_lshl_add_u32 v14, v13, 4, v9
	v_lshl_add_u32 v15, v13, 2, v10
	v_add_u32_e32 v13, 0x1600, v8
	ds_write_b128 v14, v[108:111]
	ds_write_b32 v15, v13
	s_mov_b64 exec, -1
	s_bcnt1_i32_b64 s40, vcc
	s_add_i32 s42, s42, s40
.Lsc_s22:
	s_add_u32 s40, s39, 0x800
	buffer_load_dwordx4 v[108:111], v6, s[28:31], s40 offen nt
	s_waitcnt vmcnt(19)
	v_or3_b32 v12, v112, v113, v114
	v_bitop3_b32 v12, v12, s9, v115 bitop3:0xc8
	v_cmp_ne_u32_e32 vcc, 0, v12
	s_cbranch_vccz .Lsc_s23
	s_nop 0
	v_mbcnt_lo_u32_b32 v13, vcc_lo, 0
	v_mbcnt_hi_u32_b32 v13, vcc_hi, v13
	v_add_u32_e32 v13, s42, v13
	v_cmp_gt_i32_e64 s[0:1], s7, v13
	s_and_b64 s[4:5], vcc, s[0:1]
	s_and_saveexec_b64 s[0:1], s[4:5]
	v_lshl_add_u32 v14, v13, 4, v9
	v_lshl_add_u32 v15, v13, 2, v10
	v_add_u32_e32 v13, 0x1700, v8
	ds_write_b128 v14, v[112:115]
	ds_write_b32 v15, v13
	s_mov_b64 exec, -1
	s_bcnt1_i32_b64 s40, vcc
	s_add_i32 s42, s42, s40
.Lsc_s23:
	s_add_u32 s40, s39, 0xc00
	buffer_load_dwordx4 v[112:115], v6, s[28:31], s40 offen nt
	s_waitcnt vmcnt(19)
	v_or3_b32 v12, v116, v117, v118
	v_bitop3_b32 v12, v12, s9, v119 bitop3:0xc8
	v_cmp_ne_u32_e32 vcc, 0, v12
	s_cbranch_vccz .Lsc_s24
	s_nop 0
	v_mbcnt_lo_u32_b32 v13, vcc_lo, 0
	v_mbcnt_hi_u32_b32 v13, vcc_hi, v13
	v_add_u32_e32 v13, s42, v13
	v_cmp_gt_i32_e64 s[0:1], s7, v13
	s_and_b64 s[4:5], vcc, s[0:1]
	s_and_saveexec_b64 s[0:1], s[4:5]
	v_lshl_add_u32 v14, v13, 4, v9
	v_lshl_add_u32 v15, v13, 2, v10
	v_add_u32_e32 v13, 0x1800, v8
	ds_write_b128 v14, v[116:119]
	ds_write_b32 v15, v13
	s_mov_b64 exec, -1
	s_bcnt1_i32_b64 s40, vcc
	s_add_i32 s42, s42, s40
.Lsc_s24:
	s_add_u32 s40, s39, 0x1000
	buffer_load_dwordx4 v[116:119], v6, s[28:31], s40 offen nt
	s_waitcnt vmcnt(19)
	v_or3_b32 v12, v120, v121, v122
	v_bitop3_b32 v12, v12, s9, v123 bitop3:0xc8
	v_cmp_ne_u32_e32 vcc, 0, v12
	s_cbranch_vccz .Lsc_s25
	s_nop 0
	v_mbcnt_lo_u32_b32 v13, vcc_lo, 0
	v_mbcnt_hi_u32_b32 v13, vcc_hi, v13
	v_add_u32_e32 v13, s42, v13
	v_cmp_gt_i32_e64 s[0:1], s7, v13
	s_and_b64 s[4:5], vcc, s[0:1]
	s_and_saveexec_b64 s[0:1], s[4:5]
	v_lshl_add_u32 v14, v13, 4, v9
	v_lshl_add_u32 v15, v13, 2, v10
	v_add_u32_e32 v13, 0x1900, v8
	ds_write_b128 v14, v[120:123]
	ds_write_b32 v15, v13
	s_mov_b64 exec, -1
	s_bcnt1_i32_b64 s40, vcc
	s_add_i32 s42, s42, s40
.Lsc_s25:
	s_add_u32 s40, s39, 0x1400
	buffer_load_dwordx4 v[120:123], v6, s[28:31], s40 offen nt
	s_waitcnt vmcnt(19)
	v_or3_b32 v12, v124, v125, v126
	v_bitop3_b32 v12, v12, s9, v127 bitop3:0xc8
	v_cmp_ne_u32_e32 vcc, 0, v12
	s_cbranch_vccz .Lsc_s26
	s_nop 0
	v_mbcnt_lo_u32_b32 v13, vcc_lo, 0
	v_mbcnt_hi_u32_b32 v13, vcc_hi, v13
	v_add_u32_e32 v13, s42, v13
	v_cmp_gt_i32_e64 s[0:1], s7, v13
	s_and_b64 s[4:5], vcc, s[0:1]
	s_and_saveexec_b64 s[0:1], s[4:5]
	v_lshl_add_u32 v14, v13, 4, v9
	v_lshl_add_u32 v15, v13, 2, v10
	v_add_u32_e32 v13, 0x1a00, v8
	ds_write_b128 v14, v[124:127]
	ds_write_b32 v15, v13
	s_mov_b64 exec, -1
	s_bcnt1_i32_b64 s40, vcc
	s_add_i32 s42, s42, s40
.Lsc_s26:
	s_add_u32 s40, s39, 0x1800
	buffer_load_dwordx4 v[124:127], v6, s[28:31], s40 offen nt
	s_waitcnt vmcnt(19)
	v_or3_b32 v12, v128, v129, v130
	v_bitop3_b32 v12, v12, s9, v131 bitop3:0xc8
	v_cmp_ne_u32_e32 vcc, 0, v12
	s_cbranch_vccz .Lsc_s27
	s_nop 0
	v_mbcnt_lo_u32_b32 v13, vcc_lo, 0
	v_mbcnt_hi_u32_b32 v13, vcc_hi, v13
	v_add_u32_e32 v13, s42, v13
	v_cmp_gt_i32_e64 s[0:1], s7, v13
	s_and_b64 s[4:5], vcc, s[0:1]
	s_and_saveexec_b64 s[0:1], s[4:5]
	v_lshl_add_u32 v14, v13, 4, v9
	v_lshl_add_u32 v15, v13, 2, v10
	v_add_u32_e32 v13, 0x1b00, v8
	ds_write_b128 v14, v[128:131]
	ds_write_b32 v15, v13
	s_mov_b64 exec, -1
	s_bcnt1_i32_b64 s40, vcc
	s_add_i32 s42, s42, s40
.Lsc_s27:
	s_add_u32 s40, s39, 0x1c00
	buffer_load_dwordx4 v[128:131], v6, s[28:31], s40 offen nt
	s_waitcnt vmcnt(19)
	v_or3_b32 v12, v132, v133, v134
	v_bitop3_b32 v12, v12, s9, v135 bitop3:0xc8
	v_cmp_ne_u32_e32 vcc, 0, v12
	s_cbranch_vccz .Lsc_s28
	s_nop 0
	v_mbcnt_lo_u32_b32 v13, vcc_lo, 0
	v_mbcnt_hi_u32_b32 v13, vcc_hi, v13
	v_add_u32_e32 v13, s42, v13
	v_cmp_gt_i32_e64 s[0:1], s7, v13
	s_and_b64 s[4:5], vcc, s[0:1]
	s_and_saveexec_b64 s[0:1], s[4:5]
	v_lshl_add_u32 v14, v13, 4, v9
	v_lshl_add_u32 v15, v13, 2, v10
	v_add_u32_e32 v13, 0x1c00, v8
	ds_write_b128 v14, v[132:135]
	ds_write_b32 v15, v13
	s_mov_b64 exec, -1
	s_bcnt1_i32_b64 s40, vcc
	s_add_i32 s42, s42, s40
.Lsc_s28:
	s_add_u32 s40, s39, 0x2000
	buffer_load_dwordx4 v[132:135], v6, s[28:31], s40 offen nt
	s_waitcnt vmcnt(19)
	v_or3_b32 v12, v136, v137, v138
	v_bitop3_b32 v12, v12, s9, v139 bitop3:0xc8
	v_cmp_ne_u32_e32 vcc, 0, v12
	s_cbranch_vccz .Lsc_s29
	s_nop 0
	v_mbcnt_lo_u32_b32 v13, vcc_lo, 0
	v_mbcnt_hi_u32_b32 v13, vcc_hi, v13
	v_add_u32_e32 v13, s42, v13
	v_cmp_gt_i32_e64 s[0:1], s7, v13
	s_and_b64 s[4:5], vcc, s[0:1]
	s_and_saveexec_b64 s[0:1], s[4:5]
	v_lshl_add_u32 v14, v13, 4, v9
	v_lshl_add_u32 v15, v13, 2, v10
	v_add_u32_e32 v13, 0x1d00, v8
	ds_write_b128 v14, v[136:139]
	ds_write_b32 v15, v13
	s_mov_b64 exec, -1
	s_bcnt1_i32_b64 s40, vcc
	s_add_i32 s42, s42, s40
.Lsc_s29:
	s_add_u32 s40, s39, 0x2400
	buffer_load_dwordx4 v[136:139], v6, s[28:31], s40 offen nt
	s_waitcnt vmcnt(19)
	v_or3_b32 v12, v140, v141, v142
	v_bitop3_b32 v12, v12, s9, v143 bitop3:0xc8
	v_cmp_ne_u32_e32 vcc, 0, v12
	s_cbranch_vccz .Lsc_s30
	s_nop 0
	v_mbcnt_lo_u32_b32 v13, vcc_lo, 0
	v_mbcnt_hi_u32_b32 v13, vcc_hi, v13
	v_add_u32_e32 v13, s42, v13
	v_cmp_gt_i32_e64 s[0:1], s7, v13
	s_and_b64 s[4:5], vcc, s[0:1]
	s_and_saveexec_b64 s[0:1], s[4:5]
	v_lshl_add_u32 v14, v13, 4, v9
	v_lshl_add_u32 v15, v13, 2, v10
	v_add_u32_e32 v13, 0x1e00, v8
	ds_write_b128 v14, v[140:143]
	ds_write_b32 v15, v13
	s_mov_b64 exec, -1
	s_bcnt1_i32_b64 s40, vcc
	s_add_i32 s42, s42, s40
.Lsc_s30:
	s_add_u32 s40, s39, 0x2800
	buffer_load_dwordx4 v[140:143], v6, s[28:31], s40 offen nt
	s_waitcnt vmcnt(19)
	v_or3_b32 v12, v144, v145, v146
	v_bitop3_b32 v12, v12, s9, v147 bitop3:0xc8
	v_cmp_ne_u32_e32 vcc, 0, v12
	s_cbranch_vccz .Lsc_s31
	s_nop 0
	v_mbcnt_lo_u32_b32 v13, vcc_lo, 0
	v_mbcnt_hi_u32_b32 v13, vcc_hi, v13
	v_add_u32_e32 v13, s42, v13
	v_cmp_gt_i32_e64 s[0:1], s7, v13
	s_and_b64 s[4:5], vcc, s[0:1]
	s_and_saveexec_b64 s[0:1], s[4:5]
	v_lshl_add_u32 v14, v13, 4, v9
	v_lshl_add_u32 v15, v13, 2, v10
	v_add_u32_e32 v13, 0x1f00, v8
	ds_write_b128 v14, v[144:147]
	ds_write_b32 v15, v13
	s_mov_b64 exec, -1
	s_bcnt1_i32_b64 s40, vcc
	s_add_i32 s42, s42, s40
.Lsc_s31:
	s_add_u32 s40, s39, 0x2c00
	buffer_load_dwordx4 v[144:147], v6, s[28:31], s40 offen nt
	s_waitcnt vmcnt(19)
	v_or3_b32 v12, v148, v149, v150
	v_bitop3_b32 v12, v12, s9, v151 bitop3:0xc8
	v_cmp_ne_u32_e32 vcc, 0, v12
	s_cbranch_vccz .Lsc_s32
	s_nop 0
	v_mbcnt_lo_u32_b32 v13, vcc_lo, 0
	v_mbcnt_hi_u32_b32 v13, vcc_hi, v13
	v_add_u32_e32 v13, s42, v13
	v_cmp_gt_i32_e64 s[0:1], s7, v13
	s_and_b64 s[4:5], vcc, s[0:1]
	s_and_saveexec_b64 s[0:1], s[4:5]
	v_lshl_add_u32 v14, v13, 4, v9
	v_lshl_add_u32 v15, v13, 2, v10
	v_add_u32_e32 v13, 0x2000, v8
	ds_write_b128 v14, v[148:151]
	ds_write_b32 v15, v13
	s_mov_b64 exec, -1
	s_bcnt1_i32_b64 s40, vcc
	s_add_i32 s42, s42, s40
.Lsc_s32:
	s_add_u32 s40, s39, 0x3000
	buffer_load_dwordx4 v[148:151], v6, s[28:31], s40 offen nt
	s_waitcnt vmcnt(19)
	v_or3_b32 v12, v152, v153, v154
	v_bitop3_b32 v12, v12, s9, v155 bitop3:0xc8
	v_cmp_ne_u32_e32 vcc, 0, v12
	s_cbranch_vccz .Lsc_s33
	s_nop 0
	v_mbcnt_lo_u32_b32 v13, vcc_lo, 0
	v_mbcnt_hi_u32_b32 v13, vcc_hi, v13
	v_add_u32_e32 v13, s42, v13
	v_cmp_gt_i32_e64 s[0:1], s7, v13
	s_and_b64 s[4:5], vcc, s[0:1]
	s_and_saveexec_b64 s[0:1], s[4:5]
	v_lshl_add_u32 v14, v13, 4, v9
	v_lshl_add_u32 v15, v13, 2, v10
	v_add_u32_e32 v13, 0x2100, v8
	ds_write_b128 v14, v[152:155]
	ds_write_b32 v15, v13
	s_mov_b64 exec, -1
	s_bcnt1_i32_b64 s40, vcc
	s_add_i32 s42, s42, s40
.Lsc_s33:
	s_add_u32 s40, s39, 0x3400
	buffer_load_dwordx4 v[152:155], v6, s[28:31], s40 offen nt
	s_waitcnt vmcnt(19)
	v_or3_b32 v12, v156, v157, v158
	v_bitop3_b32 v12, v12, s9, v159 bitop3:0xc8
	v_cmp_ne_u32_e32 vcc, 0, v12
	s_cbranch_vccz .Lsc_s34
	s_nop 0
	v_mbcnt_lo_u32_b32 v13, vcc_lo, 0
	v_mbcnt_hi_u32_b32 v13, vcc_hi, v13
	v_add_u32_e32 v13, s42, v13
	v_cmp_gt_i32_e64 s[0:1], s7, v13
	s_and_b64 s[4:5], vcc, s[0:1]
	s_and_saveexec_b64 s[0:1], s[4:5]
	v_lshl_add_u32 v14, v13, 4, v9
	v_lshl_add_u32 v15, v13, 2, v10
	v_add_u32_e32 v13, 0x2200, v8
	ds_write_b128 v14, v[156:159]
	ds_write_b32 v15, v13
	s_mov_b64 exec, -1
	s_bcnt1_i32_b64 s40, vcc
	s_add_i32 s42, s42, s40
.Lsc_s34:
	s_add_u32 s40, s39, 0x3800
	buffer_load_dwordx4 v[156:159], v6, s[28:31], s40 offen nt
	s_waitcnt vmcnt(19)
	v_or3_b32 v12, v160, v161, v162
	v_bitop3_b32 v12, v12, s9, v163 bitop3:0xc8
	v_cmp_ne_u32_e32 vcc, 0, v12
	s_cbranch_vccz .Lsc_s35
	s_nop 0
	v_mbcnt_lo_u32_b32 v13, vcc_lo, 0
	v_mbcnt_hi_u32_b32 v13, vcc_hi, v13
	v_add_u32_e32 v13, s42, v13
	v_cmp_gt_i32_e64 s[0:1], s7, v13
	s_and_b64 s[4:5], vcc, s[0:1]
	s_and_saveexec_b64 s[0:1], s[4:5]
	v_lshl_add_u32 v14, v13, 4, v9
	v_lshl_add_u32 v15, v13, 2, v10
	v_add_u32_e32 v13, 0x2300, v8
	ds_write_b128 v14, v[160:163]
	ds_write_b32 v15, v13
	s_mov_b64 exec, -1
	s_bcnt1_i32_b64 s40, vcc
	s_add_i32 s42, s42, s40
.Lsc_s35:
	s_add_u32 s40, s39, 0x3c00
	buffer_load_dwordx4 v[160:163], v6, s[28:31], s40 offen nt
	s_waitcnt vmcnt(19)
	v_or3_b32 v12, v164, v165, v166
	v_bitop3_b32 v12, v12, s9, v167 bitop3:0xc8
	v_cmp_ne_u32_e32 vcc, 0, v12
	s_cbranch_vccz .Lsc_s36
	s_nop 0
	v_mbcnt_lo_u32_b32 v13, vcc_lo, 0
	v_mbcnt_hi_u32_b32 v13, vcc_hi, v13
	v_add_u32_e32 v13, s42, v13
	v_cmp_gt_i32_e64 s[0:1], s7, v13
	s_and_b64 s[4:5], vcc, s[0:1]
	s_and_saveexec_b64 s[0:1], s[4:5]
	v_lshl_add_u32 v14, v13, 4, v9
	v_lshl_add_u32 v15, v13, 2, v10
	v_add_u32_e32 v13, 0x2400, v8
	ds_write_b128 v14, v[164:167]
	ds_write_b32 v15, v13
	s_mov_b64 exec, -1
	s_bcnt1_i32_b64 s40, vcc
	s_add_i32 s42, s42, s40
.Lsc_s36:
	s_add_u32 s40, s39, 0x4000
	buffer_load_dwordx4 v[164:167], v6, s[28:31], s40 offen nt
	s_waitcnt vmcnt(19)
	v_or3_b32 v12, v168, v169, v170
	v_bitop3_b32 v12, v12, s9, v171 bitop3:0xc8
	v_cmp_ne_u32_e32 vcc, 0, v12
	s_cbranch_vccz .Lsc_s37
	s_nop 0
	v_mbcnt_lo_u32_b32 v13, vcc_lo, 0
	v_mbcnt_hi_u32_b32 v13, vcc_hi, v13
	v_add_u32_e32 v13, s42, v13
	v_cmp_gt_i32_e64 s[0:1], s7, v13
	s_and_b64 s[4:5], vcc, s[0:1]
	s_and_saveexec_b64 s[0:1], s[4:5]
	v_lshl_add_u32 v14, v13, 4, v9
	v_lshl_add_u32 v15, v13, 2, v10
	v_add_u32_e32 v13, 0x2500, v8
	ds_write_b128 v14, v[168:171]
	ds_write_b32 v15, v13
	s_mov_b64 exec, -1
	s_bcnt1_i32_b64 s40, vcc
	s_add_i32 s42, s42, s40
.Lsc_s37:
	s_add_u32 s40, s39, 0x4400
	buffer_load_dwordx4 v[168:171], v6, s[28:31], s40 offen nt
	s_waitcnt vmcnt(19)
	v_or3_b32 v12, v172, v173, v174
	v_bitop3_b32 v12, v12, s9, v175 bitop3:0xc8
	v_cmp_ne_u32_e32 vcc, 0, v12
	s_cbranch_vccz .Lsc_s38
	s_nop 0
	v_mbcnt_lo_u32_b32 v13, vcc_lo, 0
	v_mbcnt_hi_u32_b32 v13, vcc_hi, v13
	v_add_u32_e32 v13, s42, v13
	v_cmp_gt_i32_e64 s[0:1], s7, v13
	s_and_b64 s[4:5], vcc, s[0:1]
	s_and_saveexec_b64 s[0:1], s[4:5]
	v_lshl_add_u32 v14, v13, 4, v9
	v_lshl_add_u32 v15, v13, 2, v10
	v_add_u32_e32 v13, 0x2600, v8
	ds_write_b128 v14, v[172:175]
	ds_write_b32 v15, v13
	s_mov_b64 exec, -1
	s_bcnt1_i32_b64 s40, vcc
	s_add_i32 s42, s42, s40
.Lsc_s38:
	s_add_u32 s40, s39, 0x4800
	buffer_load_dwordx4 v[172:175], v6, s[28:31], s40 offen nt
	s_waitcnt vmcnt(19)
	v_or3_b32 v12, v176, v177, v178
	v_bitop3_b32 v12, v12, s9, v179 bitop3:0xc8
	v_cmp_ne_u32_e32 vcc, 0, v12
	s_and_b64 vcc, vcc, s[50:51]
	s_cbranch_vccz .Lsc_s39
	s_nop 0
	v_mbcnt_lo_u32_b32 v13, vcc_lo, 0
	v_mbcnt_hi_u32_b32 v13, vcc_hi, v13
	v_add_u32_e32 v13, s42, v13
	v_cmp_gt_i32_e64 s[0:1], s7, v13
	s_and_b64 s[4:5], vcc, s[0:1]
	s_and_saveexec_b64 s[0:1], s[4:5]
	v_lshl_add_u32 v14, v13, 4, v9
	v_lshl_add_u32 v15, v13, 2, v10
	v_add_u32_e32 v13, 0x2700, v8
	ds_write_b128 v14, v[176:179]
	ds_write_b32 v15, v13
	s_mov_b64 exec, -1
	s_bcnt1_i32_b64 s40, vcc
	s_add_i32 s42, s42, s40
.Lsc_s39:
	s_add_u32 s40, s39, 0x4c00
	buffer_load_dwordx4 v[176:179], v6, s[28:31], s40 offen nt
	s_waitcnt lgkmcnt(0)
	s_add_i32 s42, s42, 1
	v_mov_b32_e32 v12, s42
	ds_write_b32 v11, v12
	s_cmp_eq_u32 s35, s36
	s_cbranch_scc1 .LBB1_384
	s_add_i32 s35, s35, 1
	s_mov_b32 s37, s52
	s_mov_b32 s38, s39
	s_mov_b32 s47, s53
	s_branch .Lsc_row

amdhsa.kernels:
  - .agpr_count:     0
    .args:
      - .actual_access:  read_only
        .address_space:  global
        .offset:         0
        .size:           8
        .value_kind:     global_buffer
      - .actual_access:  read_only
        .address_space:  global
        .offset:         8
        .size:           8
        .value_kind:     global_buffer
      - .actual_access:  write_only
        .address_space:  global
        .offset:         16
        .size:           8
        .value_kind:     global_buffer
      - .actual_access:  write_only
        .address_space:  global
        .offset:         24
        .size:           8
        .value_kind:     global_buffer
      - .offset:         32
        .size:           4
        .value_kind:     hidden_block_count_x
      - .offset:         36
        .size:           4
        .value_kind:     hidden_block_count_y
      - .offset:         40
        .size:           4
        .value_kind:     hidden_block_count_z
      - .offset:         44
        .size:           2
        .value_kind:     hidden_group_size_x
      - .offset:         46
        .size:           2
        .value_kind:     hidden_group_size_y
      - .offset:         48
        .size:           2
        .value_kind:     hidden_group_size_z
      - .offset:         50
        .size:           2
        .value_kind:     hidden_remainder_x
      - .offset:         52
        .size:           2
        .value_kind:     hidden_remainder_y
      - .offset:         54
        .size:           2
        .value_kind:     hidden_remainder_z
      - .offset:         72
        .size:           8
        .value_kind:     hidden_global_offset_x
      - .offset:         80
        .size:           8
        .value_kind:     hidden_global_offset_y
      - .offset:         88
        .size:           8
        .value_kind:     hidden_global_offset_z
      - .offset:         96
        .size:           2
        .value_kind:     hidden_grid_dims
    .group_segment_fixed_size: 0
    .kernarg_segment_align: 8
    .kernarg_segment_size: 288
    .language:       OpenCL C
    .language_version:
      - 2
      - 0
    .max_flat_workgroup_size: 256
    .name:           _Z11prep_kernelPKfS0_PfPDv4_DF16_
    .private_segment_fixed_size: 0
    .sgpr_count:     20
    .sgpr_spill_count: 0
    .symbol:         _Z11prep_kernelPKfS0_PfPDv4_DF16_.kd
    .uniform_work_group_size: 1
    .uses_dynamic_stack: false
    .vgpr_count:     17
    .vgpr_spill_count: 0
    .wavefront_size: 64
  - .agpr_count:     0
    .args:
      - .actual_access:  read_only
        .address_space:  global
        .offset:         0
        .size:           8
        .value_kind:     global_buffer
      - .actual_access:  read_only
        .address_space:  global
        .offset:         8
        .size:           8
        .value_kind:     global_buffer
      - .actual_access:  read_only
        .address_space:  global
        .offset:         16
        .size:           8
        .value_kind:     global_buffer
      - .actual_access:  read_only
        .address_space:  global
        .offset:         24
        .size:           8
        .value_kind:     global_buffer
      - .actual_access:  write_only
        .address_space:  global
        .offset:         32
        .size:           8
        .value_kind:     global_buffer
      - .offset:         40
        .size:           4
        .value_kind:     by_value
    .group_segment_fixed_size: 36896
    .kernarg_segment_align: 8
    .kernarg_segment_size: 44
    .language:       OpenCL C
    .language_version:
      - 2
      - 0
    .max_flat_workgroup_size: 512
    .name:           _Z11attn_kernelPKfS0_PKDv8_DF16_S0_Pfi
    .private_segment_fixed_size: 0
    .sgpr_count:     60
    .sgpr_spill_count: 0
    .symbol:         _Z11attn_kernelPKfS0_PKDv8_DF16_S0_Pfi.kd
    .uniform_work_group_size: 1
    .uses_dynamic_stack: false
    .vgpr_count:     248
    .vgpr_spill_count: 0
    .wavefront_size: 64
